# additionally removed redundant acquire invalidates at 5 more grid barriers (kept after prologue, O2->O3, FFN-up->down, FFN-down->next layer)
# speedup vs baseline: 1.0104x; 1.0036x over previous
; __device__ __forceinline__ int lane_id() { int l; asm volatile("v_mbcnt_lo_u32_b32 %0, -1, 0\n\tv_mbcnt_hi_u32_b32 %0, -1, %0" : "=v"(l)); return l; }
; #define PG8_WAIT_V(n) asm volatile("s_waitcnt vmcnt(" #n ")" ::: "memory")
; #define PG8_BAR __builtin_amdgcn_s_barrier()
; template <class Epi, bool ALIGN_EPI, bool SP2>
; __device__ __forceinline__ void gemm_phase(LAS unsigned char* lds, LAS float* tab, const Gemm g, const StaticOrder& S, const Epi& E, int wave_s) {
;     int tid = wave_s * 64 + lane_id(); asm volatile("" : "+v"(tid));
;     const int wid = __builtin_amdgcn_readfirstlane(tid >> 6), lane = tid & 63, wr = wid >> 2, wc = wid & 3, fr = lane & 15, fq = lane >> 4;
;     const int K = g.K, nt = K / BK, lda = g.lda;
;     unsigned voffA[2], voffB[2];
; #pragma unroll
;     for (int i = 0; i < 2; ++i) { int R, C; stage_rc(tid * 16 + i * 8192, R, C); const int Rb = Epi::PERM ? ((R & ~31) + perm32(R & 31)) : R;
;         voffA[i] = (unsigned)(R * lda + C) * 2u; voffB[i] = (unsigned)(Rb * K + C) * 2u; }
;     const size_t kstep = (size_t)(BK * 2);
;     const size_t hstepA = (size_t)HALF * lda * 2, hstepB = (size_t)HALF * K * 2;
;     const size_t tstepA = 2 * hstepA, tstepB = 2 * hstepB;
;     const unsigned ldsw = (unsigned)wid * 1024u;
;     const int aoff = lds_byte(wr * 64 + fr, fq * 8), boff = lds_byte(wc * 32 + fr, fq * 8);
;     ...
;     Unit cur, nxt; int ui = 0;
;     if (!S.next(0, cur)) return;
;     typedef typename Epi::AccV AccV; AccV acc[2][2][4][2];
; #pragma unroll
;     for (int a = 0; a < 2; ++a)
; #pragma unroll
;         for (int b = 0; b < 2; ++b)
; #pragma unroll
;             for (int m = 0; m < 4; ++m)
; #pragma unroll
;                 for (int n = 0; n < 2; ++n) acc[a][b][m][n] = AccV{};
;     bf16x8 At[4][2], B0[2][2], B1[2][2];
;     const char* cA = (const char*)g.A + (size_t)cur.pm * tstepA + (cur.hs > 0 ? hstepA : 0); const char* cB = (const char*)g.Bt + (size_t)cur.pn * tstepB;
;     if constexpr (SP2) {
;         PG8_STAGE(PG8_SB(0, 0), cB, voffB); PG8_STAGE(PG8_SB(0, 1), cB + hstepB, voffB); PG8_STAGE(PG8_SA(0, 0), cA, voffA); PG8_STAGE(PG8_SA(0, 1), cA + hstepA, voffA);
;         if (wr == 1) PG8_BAR;
;         PG8_WAIT_V(2); PG8_BAR;
;         PG8_STAGE(PG8_SB(1, 0), cB + kstep, voffB); PG8_STAGE(PG8_SA(1, 0), cA + kstep, voffA); PG8_STAGE(PG8_SB(1, 1), cB + hstepB + kstep, voffB);
;         PG8_WAIT_V(6); PG8_BAR;
.LBB0_276:
	s_or_b64 exec, exec, s[10:11]
	s_waitcnt vmcnt(0)
	s_waitcnt vmcnt(0)
.LBB0_277:
	s_or_b64 exec, exec, s[4:5]
	s_waitcnt lgkmcnt(0)
	s_barrier
	s_load_dwordx2 s[4:5], s[76:77], 0x78
	s_waitcnt lgkmcnt(0)
	v_readlane_b32 s0, v254, 55
	v_readlane_b32 s2, v255, 3
	s_load_dword s0, s[82:83], 0x0
	v_readlane_b32 s1, v254, 56
	v_readlane_b32 s3, v255, 4
	s_mov_b32 s3, s1
	v_writelane_b32 v255, s2, 3
	s_waitcnt lgkmcnt(0)
	s_ashr_i32 s0, s0, 31
	v_mbcnt_lo_u32_b32 v0, -1, 0
	v_mbcnt_hi_u32_b32 v0, -1, v0
	v_writelane_b32 v255, s3, 4
	v_readlane_b32 s2, v254, 0
	v_add_u32_e32 v2, s79, v0
	v_readlane_b32 s3, v254, 1
	v_writelane_b32 v255, s0, 9
	s_and_b64 vcc, exec, s[2:3]
	v_readfirstlane_b32 s0, v2
	s_cbranch_vccz .LBB0_295
	v_lshlrev_b32_e32 v0, 4, v2
	v_add_u32_e32 v3, 0x2000, v0
	s_waitcnt vmcnt(13)
	v_ashrrev_i32_e32 v4, 31, v3
	v_lshrrev_b32_e32 v4, 22, v4
	v_add_u32_e32 v4, v3, v4
	s_waitcnt vmcnt(11)
	v_ashrrev_i32_e32 v12, 10, v4
	v_mul_i32_i24_e32 v4, 0x400, v12
	v_sub_u32_e32 v3, v3, v4
	v_lshrrev_b32_e32 v4, 4, v3
	v_bitop3_b32 v3, v4, v3, 32 bitop3:0x6c
	v_ashrrev_i32_e32 v4, 31, v3
	v_lshrrev_b32_e32 v4, 26, v4
	v_add_u32_e32 v4, v3, v4
	v_lshlrev_b32_e32 v5, 3, v12
	v_readlane_b32 s2, v255, 3
	v_ashrrev_i32_e32 v13, 6, v4
	v_and_b32_e32 v5, -16, v5
	v_readlane_b32 s3, v255, 4
	v_add_u32_e32 v5, v13, v5
	v_and_b32_e32 v6, 3, v13
	s_mov_b32 s3, 0x3fffe0
	v_lshrrev_b32_e32 v7, 2, v5
	v_lshlrev_b32_e32 v8, 1, v5
	v_and_b32_e32 v4, 0xc0, v4
	v_and_or_b32 v6, v5, s3, v6
	v_and_b32_e32 v7, 4, v7
	v_and_b32_e32 v8, 24, v8
	v_sub_u32_e32 v3, v3, v4
	v_or3_b32 v6, v6, v7, v8
	v_lshlrev_b32_e32 v7, 5, v12
	v_ashrrev_i16_sdwa v3, v229, sext(v3) dst_sel:DWORD dst_unused:UNUSED_PAD src0_sel:DWORD src1_sel:BYTE_0
	v_and_b32_e32 v7, 32, v7
	v_bfe_i32 v14, v3, 0, 16
	v_add_lshl_u32 v3, v7, v14, 1
	v_lshl_add_u32 v130, v6, 10, v3
	v_lshl_add_u32 v132, v5, 10, v3
	v_bfe_i32 v3, v2, 27, 1
	v_lshrrev_b32_e32 v3, 22, v3
	v_add_u32_e32 v3, v0, v3
	v_and_b32_e32 v3, 0xfffffc00, v3
	v_sub_u32_e32 v0, v0, v3
	v_lshrrev_b32_e32 v3, 4, v0
	v_bitop3_b32 v0, v3, v0, 32 bitop3:0x6c
	v_ashrrev_i32_e32 v3, 31, v0
	v_lshrrev_b32_e32 v3, 26, v3
	v_add_u32_e32 v4, v0, v3
	v_ashrrev_i32_e32 v3, 31, v2
	v_lshrrev_b32_e32 v5, 26, v3
	v_add_u32_e32 v5, v2, v5
	s_add_u32 s28, s4, 0xe800000
	v_ashrrev_i32_e32 v16, 6, v5
	s_addc_u32 s29, s5, 0
	s_mul_hi_u32 s1, s2, 0x600000
	s_mul_i32 s2, s2, 0x600000
	v_lshlrev_b32_e32 v5, 3, v16
	s_add_u32 s2, s4, s2
	v_ashrrev_i32_e32 v15, 6, v4
	v_and_b32_e32 v5, -16, v5
	s_addc_u32 s1, s5, s1
	v_add_u32_e32 v5, v15, v5
	s_add_u32 s30, s2, 0xc00000
	v_and_b32_e32 v6, 3, v15
	v_lshrrev_b32_e32 v7, 2, v5
	v_lshlrev_b32_e32 v8, 1, v5
	v_and_b32_e32 v4, 0xc0, v4
	s_addc_u32 s31, s1, 0
	s_ashr_i32 s1, s0, 6
	v_and_or_b32 v6, v5, s3, v6
	v_and_b32_e32 v7, 4, v7
	v_and_b32_e32 v8, 24, v8
	v_sub_u32_e32 v0, v0, v4
	s_ashr_i32 s2, s0, 8
	s_lshl_b32 s34, s1, 10
	v_or3_b32 v6, v6, v7, v8
	v_lshlrev_b32_e32 v7, 5, v16
	v_ashrrev_i16_sdwa v0, v229, sext(v0) dst_sel:DWORD dst_unused:UNUSED_PAD src0_sel:DWORD src1_sel:BYTE_0
	v_readlane_b32 s6, v254, 35
	v_and_b32_e32 v7, 32, v7
	v_bfe_i32 v17, v0, 0, 16
	v_readlane_b32 s7, v254, 36
	s_add_u32 s24, s30, s6
	v_add_lshl_u32 v0, v7, v17, 1
	s_addc_u32 s25, s31, s7
	s_add_i32 s35, s34, 0
	v_lshl_add_u32 v134, v6, 10, v0
	s_add_i32 m0, s35, 0x10000
	v_readlane_b32 s6, v254, 33
	global_load_lds_dwordx4 v134, s[24:25]
	s_add_i32 m0, s35, 0x12000
	v_readlane_b32 s7, v254, 34
	s_add_u32 s22, s28, s6
	s_addc_u32 s23, s29, s7
	s_add_u32 s6, s24, 0x20000
	global_load_lds_dwordx4 v130, s[24:25]
	s_addc_u32 s7, s25, 0
	s_add_i32 m0, s35, 0x14000
	s_add_i32 s36, s35, 0x2000
	global_load_lds_dwordx4 v134, s[6:7]
	s_add_i32 m0, s35, 0x16000
	v_lshl_add_u32 v136, v5, 10, v0
	global_load_lds_dwordx4 v130, s[6:7]
	s_mov_b32 m0, s35
	s_add_u32 s6, s22, 0x20000
	global_load_lds_dwordx4 v136, s[22:23]
	s_mov_b32 m0, s36
	s_addc_u32 s7, s23, 0
	s_add_i32 s37, s35, 0x4000
	global_load_lds_dwordx4 v132, s[22:23]
	s_mov_b32 m0, s37
	s_add_i32 s38, s35, 0x6000
	global_load_lds_dwordx4 v136, s[6:7]
	s_mov_b32 m0, s38
	v_mov_b32_e32 v135, v1
	global_load_lds_dwordx4 v132, s[6:7]
	v_mov_b32_e32 v131, v1
	v_mov_b32_e32 v137, v1
	v_mov_b32_e32 v133, v1
	s_cmp_eq_u32 s2, 1
	v_lshl_add_u64 v[10:11], s[24:25], 0, v[134:135]
	v_lshl_add_u64 v[8:9], s[24:25], 0, v[130:131]
	v_lshl_add_u64 v[4:5], s[22:23], 0, v[136:137]
	s_cselect_b64 s[10:11], -1, 0
	s_cmp_lg_u32 s2, 1
	v_lshl_add_u64 v[6:7], s[22:23], 0, v[132:133]
	s_cbranch_scc1 .LBB0_280
	s_barrier

; __device__ __forceinline__ unsigned xb_ld(unsigned* p)              { return __hip_atomic_load(p, __ATOMIC_RELAXED, __HIP_MEMORY_SCOPE_AGENT); }
; __device__ __forceinline__ unsigned xb_add(unsigned* p, unsigned v) { return __hip_atomic_fetch_add(p, v, __ATOMIC_RELAXED, __HIP_MEMORY_SCOPE_AGENT); }
; #define XB_SPIN(cond, bar) do { unsigned _sp = 0; while (cond) { __builtin_amdgcn_s_sleep(1); \
;     if ((++_sp & 255u) == 0u) { if (xb_ld(&(bar)[XB_TMO])) break; if (_sp > XB_SPIN_CAP) { atomicAdd(&(bar)[XB_TMO], 1u); break; } } } } while (0)
; __device__ __forceinline__ void xcd_barrier_impl(const XcdBarrier& b, bool leader) {
;     ...
;         const unsigned old = xb_add(&bar[XB_XSUB(b.x)], 1u);
;         const unsigned gen = old / nloc;
;         if (old + 1u == (gen + 1u) * nloc) {
;             __builtin_amdgcn_fence(__ATOMIC_RELEASE, "agent");
;             asm volatile("s_waitcnt vmcnt(0)" ::: "memory");
;             const unsigned og = xb_add(&bar[XB_TOP], 1u);
;             const unsigned tg = og / nx;
;             if (og + 1u != (tg + 1u) * nx) XB_SPIN(xb_ld(&bar[XB_TOP]) < (tg + 1u) * nx, bar);
;             __builtin_amdgcn_fence(__ATOMIC_ACQUIRE, "agent");
;             asm volatile("s_waitcnt vmcnt(0)" ::: "memory");
;         } else {
;             XB_SPIN(xb_ld(&bar[XB_TOP]) < (gen + 1u) * nx, bar);
.LBB0_328:
	s_or_b64 exec, exec, s[12:13]
	s_waitcnt vmcnt(0)
	s_waitcnt vmcnt(0)
.LBB0_329:
	s_andn2_saveexec_b64 s[0:1], s[8:9]
	s_cbranch_execz .LBB0_346
	s_mov_b64 s[10:11], exec
	s_waitcnt lgkmcnt(0)
	s_waitcnt vmcnt(0)
	v_mbcnt_lo_u32_b32 v2, s10, 0
	s_add_u32 s8, s6, 0x7400
	v_mbcnt_hi_u32_b32 v2, s11, v2
	s_addc_u32 s9, s7, 0
	v_cmp_eq_u32_e32 vcc, 0, v2
	s_and_saveexec_b64 s[12:13], vcc
	s_cbranch_execz .LBB0_332
	s_bcnt1_i32_b64 s0, s[10:11]
	v_mov_b32_e32 v3, s0
	global_atomic_add v3, v1, v3, s[8:9] sc0

; __device__ __forceinline__ int lane_id() { int l; asm volatile("v_mbcnt_lo_u32_b32 %0, -1, 0\n\tv_mbcnt_hi_u32_b32 %0, -1, %0" : "=v"(l)); return l; }
; __device__ __forceinline__ unsigned xb_ld(unsigned* p)              { return __hip_atomic_load(p, __ATOMIC_RELAXED, __HIP_MEMORY_SCOPE_AGENT); }
; #define XB_SPIN(cond, bar) do { unsigned _sp = 0; while (cond) { __builtin_amdgcn_s_sleep(1); \
;     if ((++_sp & 255u) == 0u) { if (xb_ld(&(bar)[XB_TMO])) break; if (_sp > XB_SPIN_CAP) { atomicAdd(&(bar)[XB_TMO], 1u); break; } } } } while (0)
; __device__ __forceinline__ void xcd_barrier_impl(const XcdBarrier& b, bool leader) {
;     ...
;             __builtin_amdgcn_fence(__ATOMIC_ACQUIRE, "agent");
;             asm volatile("s_waitcnt vmcnt(0)" ::: "memory");
;         } else {
;             XB_SPIN(xb_ld(&bar[XB_TOP]) < (gen + 1u) * nx, bar);
;             __builtin_amdgcn_fence(__ATOMIC_ACQUIRE, "agent");
;             asm volatile("s_waitcnt vmcnt(0)" ::: "memory");
;         }
; __device__ __forceinline__ Frame make_frame(int wave_s) {
;     Frame F; F.lds = LDS0; { int t_ = wave_s * 64 + lane_id(); asm volatile("" : "+v"(t_)); F.tid = t_; } F.lane = F.tid & 63; F.wave = wave_s;
;     F.G = gridDim.x; { const int bx = blockIdx.x; F.vcu = (F.G % 8 == 0) ? (bx % 8) * (F.G / 8) + bx / 8 : bx; }
;     return F;
.LBB0_345:
	s_or_b64 exec, exec, s[10:11]
	s_waitcnt vmcnt(0)
	s_waitcnt vmcnt(0)
.LBB0_346:
	s_or_b64 exec, exec, s[4:5]
	s_waitcnt lgkmcnt(0)
	s_barrier
	v_mbcnt_lo_u32_b32 v0, -1, 0
	v_mbcnt_hi_u32_b32 v0, -1, v0
	s_andn2_b64 vcc, exec, s[42:43]
	v_add_u32_e32 v3, s79, v0
	s_mov_b32 s82, s74
	s_cbranch_vccnz .LBB0_348
	v_readlane_b32 s0, v255, 6
	s_ashr_i32 s0, s0, 3
	v_readlane_b32 s1, v254, 22
	s_mul_i32 s0, s0, s1
	v_readlane_b32 s1, v254, 19
	s_add_i32 s82, s0, s1

; __device__ __forceinline__ unsigned xb_ld(unsigned* p)              { return __hip_atomic_load(p, __ATOMIC_RELAXED, __HIP_MEMORY_SCOPE_AGENT); }
; __device__ __forceinline__ unsigned xb_add(unsigned* p, unsigned v) { return __hip_atomic_fetch_add(p, v, __ATOMIC_RELAXED, __HIP_MEMORY_SCOPE_AGENT); }
; #define XB_SPIN(cond, bar) do { unsigned _sp = 0; while (cond) { __builtin_amdgcn_s_sleep(1); \
;     if ((++_sp & 255u) == 0u) { if (xb_ld(&(bar)[XB_TMO])) break; if (_sp > XB_SPIN_CAP) { atomicAdd(&(bar)[XB_TMO], 1u); break; } } } } while (0)
; __device__ __forceinline__ void xcd_barrier_impl(const XcdBarrier& b, bool leader) {
;     ...
;         const unsigned old = xb_add(&bar[XB_XSUB(b.x)], 1u);
;         const unsigned gen = old / nloc;
;         if (old + 1u == (gen + 1u) * nloc) {
;             __builtin_amdgcn_fence(__ATOMIC_RELEASE, "agent");
;             asm volatile("s_waitcnt vmcnt(0)" ::: "memory");
;             const unsigned og = xb_add(&bar[XB_TOP], 1u);
;             const unsigned tg = og / nx;
;             if (og + 1u != (tg + 1u) * nx) XB_SPIN(xb_ld(&bar[XB_TOP]) < (tg + 1u) * nx, bar);
.LBB0_671:
	s_or_b64 exec, exec, s[16:17]
	s_xor_b64 s[0:1], s[18:19], -1
	s_and_saveexec_b64 s[2:3], s[0:1]
	s_xor_b64 s[2:3], exec, s[2:3]
	s_cbranch_execz .LBB0_674
	s_mov_b64 s[14:15], exec
	v_mbcnt_lo_u32_b32 v0, s14, 0
	v_mbcnt_hi_u32_b32 v0, s15, v0
	v_cmp_eq_u32_e32 vcc, 0, v0
	s_and_b64 s[0:1], exec, vcc
	s_mov_b64 exec, s[0:1]
	s_cbranch_execz .LBB0_674
	s_bcnt1_i32_b64 s0, s[14:15]
	v_mov_b32_e32 v0, s0
	global_atomic_add v1, v0, s[12:13]
.LBB0_674:
	s_or_b64 exec, exec, s[10:11]
	s_waitcnt vmcnt(0)
	s_waitcnt vmcnt(0)
.LBB0_675:
	s_andn2_saveexec_b64 s[0:1], s[8:9]
	s_cbranch_execz .LBB0_692
	s_mov_b64 s[10:11], exec
	buffer_wbl2 sc1
	s_waitcnt lgkmcnt(0)
	s_waitcnt vmcnt(0)
	v_mbcnt_lo_u32_b32 v2, s10, 0
	s_add_u32 s8, s6, 0x7400
	v_mbcnt_hi_u32_b32 v2, s11, v2
	s_addc_u32 s9, s7, 0
	v_cmp_eq_u32_e32 vcc, 0, v2
	s_and_saveexec_b64 s[12:13], vcc
	s_cbranch_execz .LBB0_678
	s_bcnt1_i32_b64 s0, s[10:11]
	v_mov_b32_e32 v3, s0
	global_atomic_add v3, v1, v3, s[8:9] sc0

; __device__ __forceinline__ int lane_id() { int l; asm volatile("v_mbcnt_lo_u32_b32 %0, -1, 0\n\tv_mbcnt_hi_u32_b32 %0, -1, %0" : "=v"(l)); return l; }
; __device__ __forceinline__ unsigned xb_ld(unsigned* p)              { return __hip_atomic_load(p, __ATOMIC_RELAXED, __HIP_MEMORY_SCOPE_AGENT); }
; #define XB_SPIN(cond, bar) do { unsigned _sp = 0; while (cond) { __builtin_amdgcn_s_sleep(1); \
;     if ((++_sp & 255u) == 0u) { if (xb_ld(&(bar)[XB_TMO])) break; if (_sp > XB_SPIN_CAP) { atomicAdd(&(bar)[XB_TMO], 1u); break; } } } } while (0)
; __device__ __forceinline__ void xcd_barrier_impl(const XcdBarrier& b, bool leader) {
;     ...
;             XB_SPIN(xb_ld(&bar[XB_TOP]) < (gen + 1u) * nx, bar);
;             __builtin_amdgcn_fence(__ATOMIC_ACQUIRE, "agent");
;             asm volatile("s_waitcnt vmcnt(0)" ::: "memory");
;         }
; __device__ __forceinline__ Frame make_frame(int wave_s) {
;     Frame F; F.lds = LDS0; { int t_ = wave_s * 64 + lane_id(); asm volatile("" : "+v"(t_)); F.tid = t_; } F.lane = F.tid & 63; F.wave = wave_s;
;     F.G = gridDim.x; { const int bx = blockIdx.x; F.vcu = (F.G % 8 == 0) ? (bx % 8) * (F.G / 8) + bx / 8 : bx; }
;     return F;
.LBB0_691:
	s_or_b64 exec, exec, s[10:11]
	s_waitcnt vmcnt(0)
	s_waitcnt vmcnt(0)
.LBB0_692:
	s_or_b64 exec, exec, s[4:5]
	s_waitcnt lgkmcnt(0)
	s_barrier
	v_mbcnt_lo_u32_b32 v0, -1, 0
	v_mbcnt_hi_u32_b32 v0, -1, v0
	s_mov_b32 s57, s74
	v_add_u32_e32 v212, s79, v0
	s_load_dword s56, s[82:83], 0x0
	s_waitcnt lgkmcnt(0)
	s_and_b32 s0, s56, 7
	s_cmp_eq_u32 s0, 0
	s_cselect_b64 s[24:25], -1, 0
	s_cmp_lg_u32 s0, 0
	s_cbranch_scc1 .LBB0_694
	s_ashr_i32 s0, s56, 3
	v_readlane_b32 s1, v254, 22
	s_mul_i32 s0, s0, s1
	v_readlane_b32 s1, v254, 19
	s_add_i32 s57, s0, s1

; __device__ __forceinline__ unsigned xb_ld(unsigned* p)              { return __hip_atomic_load(p, __ATOMIC_RELAXED, __HIP_MEMORY_SCOPE_AGENT); }
; __device__ __forceinline__ unsigned xb_add(unsigned* p, unsigned v) { return __hip_atomic_fetch_add(p, v, __ATOMIC_RELAXED, __HIP_MEMORY_SCOPE_AGENT); }
; #define XB_SPIN(cond, bar) do { unsigned _sp = 0; while (cond) { __builtin_amdgcn_s_sleep(1); \
;     if ((++_sp & 255u) == 0u) { if (xb_ld(&(bar)[XB_TMO])) break; if (_sp > XB_SPIN_CAP) { atomicAdd(&(bar)[XB_TMO], 1u); break; } } } } while (0)
; __device__ __forceinline__ void xcd_barrier_impl(const XcdBarrier& b, bool leader) {
;     ...
;         const unsigned old = xb_add(&bar[XB_XSUB(b.x)], 1u);
;         const unsigned gen = old / nloc;
;         if (old + 1u == (gen + 1u) * nloc) {
;             __builtin_amdgcn_fence(__ATOMIC_RELEASE, "agent");
;             asm volatile("s_waitcnt vmcnt(0)" ::: "memory");
;             const unsigned og = xb_add(&bar[XB_TOP], 1u);
;             const unsigned tg = og / nx;
;             if (og + 1u != (tg + 1u) * nx) XB_SPIN(xb_ld(&bar[XB_TOP]) < (tg + 1u) * nx, bar);
;             __builtin_amdgcn_fence(__ATOMIC_ACQUIRE, "agent");
;             asm volatile("s_waitcnt vmcnt(0)" ::: "memory");
;         } else {
;             XB_SPIN(xb_ld(&bar[XB_TOP]) < (gen + 1u) * nx, bar);
.LBB0_1828:
	s_or_b64 exec, exec, s[12:13]
	s_waitcnt vmcnt(0)
	s_waitcnt vmcnt(0)
.LBB0_1829:
	s_andn2_saveexec_b64 s[0:1], s[8:9]
	s_cbranch_execz .LBB0_1846
	s_mov_b64 s[10:11], exec
	s_waitcnt lgkmcnt(0)
	s_waitcnt vmcnt(0)
	v_mbcnt_lo_u32_b32 v2, s10, 0
	s_add_u32 s8, s6, 0x7400
	v_mbcnt_hi_u32_b32 v2, s11, v2
	s_addc_u32 s9, s7, 0
	v_cmp_eq_u32_e32 vcc, 0, v2
	s_and_saveexec_b64 s[12:13], vcc
	s_cbranch_execz .LBB0_1832
	s_bcnt1_i32_b64 s0, s[10:11]
	v_mov_b32_e32 v3, s0
	global_atomic_add v3, v1, v3, s[8:9] sc0

; template <int I> __device__ __forceinline__ const float* karg_in() { return (const float*)(const GAS float*)karg_u64<I>(); }
; __device__ __forceinline__ float* karg_out() { return (float*)(GAS float*)karg_u64<14>(); }
; __device__ __forceinline__ unsigned char* karg_ws() { return (unsigned char*)(GAS unsigned char*)karg_u64<15>(); }
; __global__ void __launch_bounds__(512, 2) trunk_fwd(Args args) {
;     ...
;             grid_barrier(wave_s);
;             { unsigned char* ws = karg_ws(); float* OUT = karg_out();
;               pg8::Gemm g{(const bf16_t*)(ws + WS_EMIX), (const bf16_t*)(ws + WS_W_EOUT + li * SZ_SQ), D, D, D, nullptr};
;               pg8::EpiRes E{(layer == 0) ? karg_in<0>() : (const float*)nullptr, (float*)nullptr, ws, false};
.LBB0_1845:
	s_or_b64 exec, exec, s[10:11]
	s_waitcnt vmcnt(0)
	s_waitcnt vmcnt(0)
.LBB0_1846:
	s_or_b64 exec, exec, s[4:5]
	s_waitcnt lgkmcnt(0)
	s_barrier
	s_load_dwordx2 s[6:7], s[76:77], 0x78
	s_waitcnt lgkmcnt(0)
	s_load_dwordx2 s[0:1], s[76:77], 0x70
	s_waitcnt lgkmcnt(0)
	s_mov_b64 s[10:11], 0
	v_readlane_b32 s0, v255, 5
	s_cmp_eq_u32 s0, 0
	s_cbranch_scc0 .LBB0_1848
	s_load_dwordx2 s[10:11], s[76:77], 0
	s_waitcnt lgkmcnt(0)

; __device__ __forceinline__ unsigned xb_ld(unsigned* p)              { return __hip_atomic_load(p, __ATOMIC_RELAXED, __HIP_MEMORY_SCOPE_AGENT); }
; #define XB_SPIN(cond, bar) do { unsigned _sp = 0; while (cond) { __builtin_amdgcn_s_sleep(1); \
;     if ((++_sp & 255u) == 0u) { if (xb_ld(&(bar)[XB_TMO])) break; if (_sp > XB_SPIN_CAP) { atomicAdd(&(bar)[XB_TMO], 1u); break; } } } } while (0)
; __device__ __forceinline__ void xcd_barrier_impl(const XcdBarrier& b, bool leader) {
;     ...
;             XB_SPIN(xb_ld(&bar[XB_TOP]) < (gen + 1u) * nx, bar);
;             __builtin_amdgcn_fence(__ATOMIC_ACQUIRE, "agent");
;             asm volatile("s_waitcnt vmcnt(0)" ::: "memory");
.LBB0_2042:
	s_or_b64 exec, exec, s[14:15]
	s_waitcnt vmcnt(0)
	s_waitcnt vmcnt(0)

;     __device__ bool next(int i, Unit& u) const {
;         u.hs = -1; long L = (long)i * G + c;
;         if (i == htail) { L = (long)i * G + (c & (G / 2 - 1)); u.hs = c / (G / 2); }
; template <class Epi> __device__ __forceinline__ void run_gemm(const pg8::Gemm& g, const Epi& E, int wave_s, bool half_tail = false) {
;     pg8::StaticOrder S; S.init(M, g.N, (int)gridDim.x, (int)blockIdx.x);
;     if (half_tail && S.nwg % S.G == S.G / 2) S.htail = S.nwg / S.G;
.LBB0_2056:
	s_or_b64 exec, exec, s[14:15]
	s_xor_b64 s[0:1], s[16:17], -1
	s_and_saveexec_b64 s[2:3], s[0:1]
	s_xor_b64 s[2:3], exec, s[2:3]
	s_cbranch_execz .LBB0_2059
	s_mov_b64 s[10:11], exec
	v_mbcnt_lo_u32_b32 v0, s10, 0
	v_mbcnt_hi_u32_b32 v0, s11, v0
	v_cmp_eq_u32_e32 vcc, 0, v0
	s_and_b64 s[0:1], exec, vcc
	s_mov_b64 exec, s[0:1]
	s_cbranch_execz .LBB0_2059
	s_bcnt1_i32_b64 s0, s[10:11]
	v_mov_b32_e32 v0, s0
	global_atomic_add v1, v0, s[8:9]
.LBB0_2059:
	s_or_b64 exec, exec, s[12:13]
	s_waitcnt vmcnt(0)
	s_waitcnt vmcnt(0)
.LBB0_2060:
	s_or_b64 exec, exec, s[6:7]
	s_abs_i32 s0, s52
	s_waitcnt lgkmcnt(0)
	v_cvt_f32_u32_e32 v0, s0
	s_sub_i32 s1, 0, s0
	s_ashr_i32 s53, s52, 31
	v_rcp_iflag_f32_e32 v0, v0
	s_barrier
	s_load_dwordx2 s[8:9], s[76:77], 0x78
	s_waitcnt lgkmcnt(0)
	v_mul_f32_e32 v0, 0x4f7ffffe, v0
	v_cvt_u32_f32_e32 v0, v0
	s_mov_b32 s66, -1
	v_readfirstlane_b32 s2, v0
	s_mul_i32 s1, s1, s2
	s_mul_hi_u32 s1, s2, s1
	s_add_i32 s2, s2, s1
	s_mul_hi_u32 s1, s2, 0x580
	s_mul_i32 s2, s1, s0
	s_sub_i32 s2, 0x580, s2
	s_add_i32 s3, s1, 1
	s_sub_i32 s6, s2, s0
	s_cmp_ge_u32 s2, s0
	s_cselect_b32 s1, s3, s1
	s_cselect_b32 s2, s6, s2
	s_add_i32 s3, s1, 1
	s_cmp_ge_u32 s2, s0
	s_cselect_b32 s0, s3, s1
	s_xor_b32 s0, s0, s53
	s_sub_i32 s2, s0, s53
	s_lshr_b32 s1, s52, 31
	s_mul_i32 s0, s2, s52
	s_sub_i32 s3, 0x580, s0
	s_add_i32 s0, s52, s1
	s_ashr_i32 s0, s0, 1
	s_add_i32 s1, s0, -1
	s_and_b32 s12, s1, s74
	s_cmp_eq_u32 s3, s0
	s_cselect_b32 s42, s2, -1
	v_mbcnt_lo_u32_b32 v0, -1, 0
	v_mbcnt_hi_u32_b32 v0, -1, v0
	s_cmp_eq_u32 s42, 0
	v_add_u32_e32 v2, s79, v0
	s_mov_b32 s2, s74
	v_readfirstlane_b32 s1, v2
	s_cbranch_scc1 .LBB0_2063
	s_cmpk_lt_i32 s2, 0x580
	s_cselect_b64 s[6:7], -1, 0
	s_cmpk_gt_i32 s2, 0x57f
	s_cbranch_scc1 .LBB0_2064
